# layer-0 MoBA attention, even tiles, keys 0..31: V^T fragment pairs of the 8 P.V MFMAs read up front into idle registers with counted lgkmcnt waits (was one LDS round trip per MFMA)
# speedup vs baseline: 1.0023x; 1.0023x over previous
.LBB0_720:
	ds_read_b64_tr_b16 v[206:207], v178 offset:38912
	ds_read_b64_tr_b16 v[208:209], v178 offset:41472
	ds_read_b64_tr_b16 v[210:211], v178 offset:44032
	ds_read_b64_tr_b16 v[212:213], v178 offset:46592
	ds_read_b64_tr_b16 v[214:215], v178 offset:38976
	ds_read_b64_tr_b16 v[216:217], v178 offset:41536
	ds_read_b64_tr_b16 v[218:219], v178 offset:44096
	ds_read_b64_tr_b16 v[220:221], v178 offset:46656
	ds_read_b64_tr_b16 v[222:223], v178 offset:39040
	ds_read_b64_tr_b16 v[224:225], v178 offset:41600
	ds_read_b64_tr_b16 v[226:227], v178 offset:44160
	ds_read_b64_tr_b16 v[228:229], v178 offset:46720
	ds_read_b64_tr_b16 v[230:231], v178 offset:39104
	ds_read_b64_tr_b16 v[232:233], v178 offset:41664
	v_sub_f32_e32 v83, v83, v195
	v_sub_f32_e32 v84, v84, v195
	v_sub_f32_e32 v85, v85, v195
	v_sub_f32_e32 v86, v86, v195
	v_sub_f32_e32 v87, v87, v195
	v_sub_f32_e32 v88, v88, v195
	v_sub_f32_e32 v89, v89, v195
	v_sub_f32_e32 v90, v90, v195
	v_exp_f32_e32 v83, v83
	v_exp_f32_e32 v84, v84
	v_exp_f32_e32 v85, v85
	v_exp_f32_e32 v86, v86
	v_exp_f32_e32 v87, v87
	v_exp_f32_e32 v88, v88
	v_exp_f32_e32 v89, v89
	v_exp_f32_e32 v90, v90
	v_cvt_pk_bf16_f32 v198, v83, v84
	v_cvt_pk_bf16_f32 v199, v85, v86
	v_cvt_pk_bf16_f32 v200, v87, v88
	v_cvt_pk_bf16_f32 v201, v89, v90
	v_sub_f32_e32 v91, v91, v195
	v_sub_f32_e32 v92, v92, v195
	s_waitcnt lgkmcnt(12)
	v_mfma_f32_32x32x16_bf16 v[48:63], v[206:209], v[198:201], v[48:63]
	ds_read_b64_tr_b16 v[206:207], v178 offset:44224
	ds_read_b64_tr_b16 v[208:209], v178 offset:46784
	v_sub_f32_e32 v93, v93, v195
	v_sub_f32_e32 v94, v94, v195
	v_sub_f32_e32 v95, v95, v195
	v_sub_f32_e32 v96, v96, v195
	v_sub_f32_e32 v97, v97, v195
	v_sub_f32_e32 v196, v196, v195
	v_exp_f32_e32 v91, v91
	v_exp_f32_e32 v92, v92
	v_exp_f32_e32 v93, v93
	v_exp_f32_e32 v94, v94
	v_exp_f32_e32 v95, v95
	v_exp_f32_e32 v96, v96
	v_exp_f32_e32 v97, v97
	v_exp_f32_e32 v196, v196
	v_cvt_pk_bf16_f32 v202, v91, v92
	v_cvt_pk_bf16_f32 v203, v93, v94
	v_cvt_pk_bf16_f32 v204, v95, v96
	v_cvt_pk_bf16_f32 v205, v97, v196
	s_and_b64 vcc, exec, s[6:7]
	s_waitcnt lgkmcnt(12)
	v_mfma_f32_32x32x16_bf16 v[48:63], v[210:213], v[202:205], v[48:63]
	s_waitcnt lgkmcnt(10)
	v_mfma_f32_32x32x16_bf16 v[32:47], v[214:217], v[198:201], v[32:47]
	s_waitcnt lgkmcnt(8)
	v_mfma_f32_32x32x16_bf16 v[32:47], v[218:221], v[202:205], v[32:47]
	s_waitcnt lgkmcnt(6)
	v_mfma_f32_32x32x16_bf16 v[16:31], v[222:225], v[198:201], v[16:31]
	s_waitcnt lgkmcnt(4)
	v_mfma_f32_32x32x16_bf16 v[16:31], v[226:229], v[202:205], v[16:31]
	s_waitcnt lgkmcnt(2)
	v_mfma_f32_32x32x16_bf16 v[0:15], v[230:233], v[198:201], v[0:15]
	s_waitcnt lgkmcnt(0)
	v_mfma_f32_32x32x16_bf16 v[0:15], v[206:209], v[202:205], v[0:15]
	s_cbranch_vccnz .LBB0_722
	v_subrev_u32_e32 v197, 32, v194
	v_cmp_lt_i32_e32 vcc, v175, v197
	s_nop 1
	v_cndmask_b32_e32 v67, v169, v67, vcc
	v_cmp_le_i32_e32 vcc, v175, v197
	s_nop 1
	v_cndmask_b32_e32 v66, v169, v66, vcc
	v_cmp_le_i32_e32 vcc, v180, v197
	s_nop 1
	v_cndmask_b32_e32 v68, v169, v68, vcc
	v_cmp_le_i32_e32 vcc, v181, v197
	s_nop 1
	v_cndmask_b32_e32 v69, v169, v69, vcc
	v_cmp_le_i32_e32 vcc, v182, v197
	s_nop 1
	v_cndmask_b32_e32 v70, v169, v70, vcc
	v_cmp_le_i32_e32 vcc, v183, v197
	s_nop 1
	v_cndmask_b32_e32 v71, v169, v71, vcc
	v_cmp_le_i32_e32 vcc, v184, v197
	s_nop 1
	v_cndmask_b32_e32 v72, v169, v72, vcc
	v_cmp_le_i32_e32 vcc, v185, v197
	s_nop 1
	v_cndmask_b32_e32 v73, v169, v73, vcc
	v_cmp_le_i32_e32 vcc, v186, v197
	s_nop 1
	v_cndmask_b32_e32 v74, v169, v74, vcc
	v_cmp_le_i32_e32 vcc, v187, v197
	s_nop 1
	v_cndmask_b32_e32 v75, v169, v75, vcc
	v_cmp_le_i32_e32 vcc, v188, v197
	s_nop 1
	v_cndmask_b32_e32 v76, v169, v76, vcc
	v_cmp_le_i32_e32 vcc, v189, v197
	s_nop 1
	v_cndmask_b32_e32 v77, v169, v77, vcc
	v_cmp_le_i32_e32 vcc, v190, v197
	s_nop 1
	v_cndmask_b32_e32 v78, v169, v78, vcc
	v_cmp_le_i32_e32 vcc, v191, v197
	s_nop 1
	v_cndmask_b32_e32 v79, v169, v79, vcc
	v_cmp_le_i32_e32 vcc, v192, v197
	s_nop 1
	v_cndmask_b32_e32 v80, v169, v80, vcc
	v_cmp_le_i32_e32 vcc, v193, v197
	s_nop 1
	v_cndmask_b32_e32 v81, v169, v81, vcc
